# speedup vs baseline: 1.0039x; 1.0039x over previous
_Z6gemm_gILi64ELi128ELi32ELi64ELi0ELi2ELi64ELi3EEv5GemmP:
	s_lshl_b32 s90, s3, 7
	s_add_u32 s90, s90, s2
	s_bfe_u32 s3, s90, 0x30003
	s_lshr_b32 s91, s90, 6
	s_lshl_b32 s91, s91, 3
	s_and_b32 s2, s90, 7
	s_or_b32 s2, s2, s91
	s_load_dword s8, s[0:1], 0x38
	s_load_dwordx4 s[4:7], s[0:1], 0x0
	v_lshrrev_b32_e32 v14, 3, v0
	v_xor_b32_e32 v1, v14, v0
	s_lshl_b32 s12, s2, 6
	v_lshlrev_b32_e32 v1, 3, v1
	v_and_b32_e32 v6, 56, v1
	v_or_b32_e32 v1, s12, v14
	s_waitcnt lgkmcnt(0)
	v_mad_u64_u32 v[2:3], s[14:15], v1, s8, v[6:7]
	v_or_b32_e32 v1, 0x100, v0
	v_lshrrev_b32_e32 v1, 3, v1
	v_xor_b32_e32 v3, v1, v0
	v_lshlrev_b32_e32 v3, 3, v3
	v_and_b32_e32 v8, 56, v3
	v_or_b32_e32 v3, s12, v1
	s_lshl_b32 s13, s3, 7
	v_mad_u64_u32 v[4:5], s[14:15], v3, s8, v[8:9]
	v_or_b32_e32 v3, s13, v14
	v_mad_i64_i32 v[10:11], s[2:3], v3, s8, 0
	v_lshl_add_u64 v[10:11], v[10:11], 1, s[6:7]
	v_lshlrev_b32_e32 v12, 1, v6
	v_mov_b32_e32 v13, 0
	v_or_b32_e32 v3, s13, v1
	v_lshl_add_u64 v[6:7], v[10:11], 0, v[12:13]
	v_mad_i64_i32 v[10:11], s[2:3], v3, s8, 0
	v_or_b32_e32 v3, 0x200, v0
	v_lshrrev_b32_e32 v15, 3, v3
	v_xor_b32_e32 v3, v15, v0
	v_lshl_add_u64 v[10:11], v[10:11], 1, s[6:7]
	v_lshlrev_b32_e32 v12, 1, v8
	v_lshlrev_b32_e32 v3, 4, v3
	v_lshl_add_u64 v[8:9], v[10:11], 0, v[12:13]
	v_and_b32_e32 v12, 0x70, v3
	v_or_b32_e32 v3, 0x300, v0
	v_or_b32_e32 v5, s13, v15
	v_lshrrev_b32_e32 v16, 3, v3
	v_mad_i64_i32 v[10:11], s[2:3], v5, s8, 0
	v_xor_b32_e32 v3, v16, v0
	v_or_b32_e32 v5, s13, v16
	s_ashr_i32 s9, s8, 31
	v_readfirstlane_b32 s10, v0
	v_lshl_add_u64 v[10:11], v[10:11], 1, s[6:7]
	v_mad_i64_i32 v[18:19], s[2:3], v5, s8, 0
	v_lshlrev_b32_e32 v3, 4, v3
	v_cmp_gt_i64_e64 s[16:17], s[8:9], 63
	v_lshl_add_u64 v[10:11], v[10:11], 0, v[12:13]
	v_lshl_add_u64 v[18:19], v[18:19], 1, s[6:7]
	v_and_b32_e32 v12, 0x70, v3
	s_lshl_b32 s2, s10, 4
	v_lshl_add_u64 v[12:13], v[18:19], 0, v[12:13]
	s_and_b32 s15, s2, 0xfffffc00
	s_mov_b32 s6, 0
	s_and_b64 vcc, exec, s[16:17]
	s_cbranch_vccz .LBB8_2
	v_ashrrev_i32_e32 v3, 31, v2
	s_mov_b32 m0, s15
	v_lshl_add_u64 v[18:19], v[2:3], 1, s[4:5]
	v_ashrrev_i32_e32 v5, 31, v4
	global_load_lds_dwordx4 v[18:19], off
	v_lshl_add_u64 v[18:19], v[4:5], 1, s[4:5]
	s_add_i32 m0, s15, 0x1000
	s_mov_b32 s6, 64
	global_load_lds_dwordx4 v[18:19], off
	s_add_i32 m0, s15, 0x2000
	s_nop 0
	global_load_lds_dwordx4 v[6:7], off
	s_add_i32 m0, s15, 0x3000
	s_nop 0
	global_load_lds_dwordx4 v[8:9], off
	s_add_i32 m0, s15, 0x4000
	s_nop 0
	global_load_lds_dwordx4 v[10:11], off
	s_add_i32 m0, s15, 0x5000
	s_nop 0
	global_load_lds_dwordx4 v[12:13], off
